# forgetting-attention items: stagger barriers removed so both wave halves run their merged MFMA+VALU segment in the same interval
# speedup vs baseline: 1.0071x; 1.0071x over previous
.LBB0_508:
	v_pk_add_f32 v[0:1], v[0:1], v[16:17] op_sel_hi:[1,0]
	v_pk_add_f32 v[2:3], v[2:3], v[16:17] op_sel_hi:[1,0]
	v_pk_mul_f32 v[18:19], v[0:1], s[88:89] op_sel_hi:[1,0]
	v_pk_add_f32 v[0:1], v[4:5], v[16:17] op_sel_hi:[1,0]
	v_pk_mul_f32 v[2:3], v[2:3], s[88:89] op_sel_hi:[1,0]
	v_pk_mul_f32 v[20:21], v[0:1], s[88:89] op_sel_hi:[1,0]
	v_pk_add_f32 v[0:1], v[6:7], v[16:17] op_sel_hi:[1,0]
	s_sub_i32 s15, 63, s59
	v_pk_mul_f32 v[0:1], v[0:1], s[88:89] op_sel_hi:[1,0]
	ds_write_b128 v114, v[0:3] offset:16
	v_pk_add_f32 v[0:1], v[8:9], v[16:17] op_sel_hi:[1,0]
	v_pk_add_f32 v[2:3], v[10:11], v[16:17] op_sel_hi:[1,0]
	v_pk_mul_f32 v[0:1], v[0:1], s[88:89] op_sel_hi:[1,0]
	v_pk_mul_f32 v[2:3], v[2:3], s[88:89] op_sel_hi:[1,0]
	ds_write_b128 v114, v[0:3] offset:32
	v_pk_add_f32 v[0:1], v[12:13], v[16:17] op_sel_hi:[1,0]
	v_pk_add_f32 v[2:3], v[14:15], v[16:17] op_sel_hi:[1,0]
	v_pk_mul_f32 v[0:1], v[0:1], s[88:89] op_sel_hi:[1,0]
	v_pk_mul_f32 v[2:3], v[2:3], s[88:89] op_sel_hi:[1,0]
	ds_write_b128 v114, v[18:21]
	ds_write_b128 v114, v[0:3] offset:48
	s_waitcnt lgkmcnt(0)
	s_barrier
	s_load_dwordx2 s[0:1], s[76:77], 0x108
	s_load_dwordx2 s[50:51], s[76:77], 0x138
	v_mov_b32_e32 v126, v108
	s_lshl_b32 s14, s15, 7
	s_add_i32 s10, s14, s89
	v_and_b32_e32 v32, 15, v126
	v_or_b32_e32 v125, s10, v32
	v_readlane_b32 s10, v247, 36
	s_lshl_b32 s62, s10, 1
	s_waitcnt lgkmcnt(0)
	s_add_u32 s48, s0, s62
	v_and_b32_e32 v0, -16, v126
	s_addc_u32 s49, s1, 0
	v_mad_u64_u32 v[8:9], s[0:1], v125, s75, v[0:1]
	v_add_u32_e32 v4, 64, v8
	v_add_u32_e32 v9, 0x80, v8
	v_add_u32_e32 v12, 0xc0, v8
	global_load_dwordx4 v[0:3], v8, s[48:49] offset:3072
	s_nop 0
	global_load_dwordx4 v[4:7], v4, s[48:49] offset:3072
	s_nop 0
	global_load_dwordx4 v[8:11], v9, s[48:49] offset:3072
	s_nop 0
	global_load_dwordx4 v[12:15], v12, s[48:49] offset:3072
	v_lshl_add_u32 v16, v125, 2, s85
	ds_read_b32 v127, v16
	s_lshl_b32 s68, s15, 1
	s_add_u32 s0, s48, 0x1000
	s_addc_u32 s1, s49, 0
	s_or_b32 s16, s68, 1
	s_add_u32 s52, s48, 0x1400
	s_addc_u32 s53, s49, 0
	s_waitcnt lgkmcnt(0)
	s_waitcnt lgkmcnt(0)
	s_barrier
	s_mul_i32 s17, s16, 0x178000
	s_add_u32 s10, s0, s17
	s_addc_u32 s11, s1, 0
	v_lshl_add_u64 v[20:21], s[10:11], 0, v[104:105]
	global_load_dwordx4 v[16:19], v[20:21], off
	v_add_co_u32_e32 v20, vcc, s86, v20
	v_add_u32_e32 v100, 0, v110
	s_nop 0
	v_addc_co_u32_e32 v21, vcc, 0, v21, vcc
	global_load_dwordx4 v[20:23], v[20:21], off
	v_add_u32_e32 v124, 0, v111
	s_waitcnt vmcnt(1)
	ds_write_b128 v100, v[16:19]
	s_waitcnt vmcnt(0)
	ds_write_b128 v124, v[20:23]
	s_waitcnt lgkmcnt(0)
	s_waitcnt lgkmcnt(0)
	s_barrier
	v_cndmask_b32_e64 v24, 0, 1, s[82:83]
	v_cmp_ne_u32_e64 s[10:11], 1, v24
	s_andn2_b64 vcc, exec, s[82:83]
	s_mul_i32 s15, s15, 0x2f0000
	s_cbranch_vccnz .LBB0_510
	s_add_u32 s12, s0, s15
	s_addc_u32 s13, s1, 0
	v_lshl_add_u64 v[16:17], s[12:13], 0, v[104:105]
	s_add_u32 s12, s52, s17
	v_add_co_u32_e32 v20, vcc, 0xbc000, v16
	s_addc_u32 s13, s53, 0
	s_nop 0
	v_addc_co_u32_e32 v21, vcc, 0, v17, vcc
	v_lshl_add_u64 v[24:25], s[12:13], 0, v[104:105]
	v_add_co_u32_e32 v28, vcc, 0xbc000, v24
	global_load_dwordx4 v[16:19], v[16:17], off
	s_nop 0
	global_load_dwordx4 v[20:23], v[20:21], off
	v_addc_co_u32_e32 v29, vcc, 0, v25, vcc
	global_load_dwordx4 v[24:27], v[24:25], off
	s_nop 0
	global_load_dwordx4 v[28:31], v[28:29], off
	s_waitcnt lgkmcnt(0)
.LBB0_510:
	v_cndmask_b32_e64 v33, 0, 1, s[80:81]
	v_cmp_ne_u32_e64 s[12:13], 1, v33
	s_andn2_b64 vcc, exec, s[80:81]
	s_cbranch_vccnz .LBB0_512
	s_add_u32 s18, s0, s15
	s_addc_u32 s19, s1, 0
	s_waitcnt vmcnt(3)
	v_lshl_add_u64 v[16:17], s[18:19], 0, v[104:105]
	s_add_u32 s18, s52, s17
	s_waitcnt vmcnt(2)
	v_add_co_u32_e32 v20, vcc, 0xbc000, v16
	s_addc_u32 s19, s53, 0
	s_nop 0
	v_addc_co_u32_e32 v21, vcc, 0, v17, vcc
	s_waitcnt vmcnt(1)
	v_lshl_add_u64 v[24:25], s[18:19], 0, v[104:105]
	s_waitcnt vmcnt(0)
	v_add_co_u32_e32 v28, vcc, 0xbc000, v24
	global_load_dwordx4 v[16:19], v[16:17], off
	s_nop 0
	global_load_dwordx4 v[20:23], v[20:21], off
	v_addc_co_u32_e32 v29, vcc, 0, v25, vcc
	global_load_dwordx4 v[24:27], v[24:25], off
	s_nop 0
	global_load_dwordx4 v[28:31], v[28:29], off

.LBB0_544:
	s_and_b64 vcc, exec, s[80:81]
	s_cbranch_vccz .LBB0_546
	s_waitcnt lgkmcnt(0)
.LBB0_546:
	ds_read_b64_tr_b16 v[0:1], v142 offset:49152
	ds_read_b64_tr_b16 v[2:3], v146 offset:49152
	ds_read_b64_tr_b16 v[6:7], v146 offset:57344
	ds_read_b64_tr_b16 v[4:5], v142 offset:57344
	ds_read_b64_tr_b16 v[8:9], v136 offset:49152
	ds_read_b64_tr_b16 v[10:11], v137 offset:49152
	ds_read_b64_tr_b16 v[14:15], v137 offset:57344
	ds_read_b64_tr_b16 v[12:13], v136 offset:57344
	s_waitcnt lgkmcnt(6)
	v_mfma_f32_16x16x32_bf16 v[0:3], v[0:3], v[68:71], v[60:63]
	s_waitcnt lgkmcnt(2)
	v_mfma_f32_16x16x32_bf16 v[8:11], v[8:11], v[68:71], v[52:55]
	v_mfma_f32_16x16x32_bf16 v[0:3], v[4:7], v[64:67], v[0:3]
	ds_read_b64_tr_b16 v[4:5], v139 offset:49152
	ds_read_b64_tr_b16 v[6:7], v145 offset:49152
	s_waitcnt lgkmcnt(2)
	v_mfma_f32_16x16x32_bf16 v[8:11], v[12:15], v[64:67], v[8:11]
	ds_read_b64_tr_b16 v[14:15], v145 offset:57344
	ds_read_b64_tr_b16 v[12:13], v139 offset:57344
	s_waitcnt vmcnt(3)
	ds_read_b64_tr_b16 v[16:17], v140 offset:49152
	ds_read_b64_tr_b16 v[18:19], v147 offset:49152
	s_waitcnt lgkmcnt(4)
	v_mfma_f32_16x16x32_bf16 v[4:7], v[4:7], v[68:71], v[48:51]
	s_waitcnt lgkmcnt(2)
	v_mfma_f32_16x16x32_bf16 v[4:7], v[12:15], v[64:67], v[4:7]
	ds_read_b64_tr_b16 v[14:15], v147 offset:57344
	ds_read_b64_tr_b16 v[12:13], v140 offset:57344
	s_waitcnt vmcnt(2)
	ds_read_b64_tr_b16 v[20:21], v148 offset:49152
	ds_read_b64_tr_b16 v[22:23], v149 offset:49152
	s_waitcnt vmcnt(1)
	ds_read_b64_tr_b16 v[26:27], v149 offset:57344
	ds_read_b64_tr_b16 v[24:25], v148 offset:57344
	v_lshlrev_b32_e32 v48, 2, v126
	s_waitcnt lgkmcnt(6)
	v_mfma_f32_16x16x32_bf16 v[16:19], v[16:19], v[68:71], v[56:59]
	s_waitcnt vmcnt(0)
	v_xor_b32_e32 v28, 64, v48
	v_mov_b32_e32 v126, v108
	s_waitcnt lgkmcnt(2)
	v_mfma_f32_16x16x32_bf16 v[20:23], v[20:23], v[68:71], v[32:35]
	s_nop 2
	ds_bpermute_b32 v32, v28, v150
	v_mfma_f32_16x16x32_bf16 v[12:15], v[12:15], v[64:67], v[16:19]
	s_nop 2
	ds_read_b64_tr_b16 v[16:17], v133 offset:49152
	ds_read_b64_tr_b16 v[18:19], v134 offset:49152
	ds_read_b64_tr_b16 v[30:31], v134 offset:57344
	ds_read_b64_tr_b16 v[28:29], v133 offset:57344
	s_waitcnt lgkmcnt(4)
	v_add_f32_e32 v49, v150, v32
	v_xor_b32_e32 v32, 0x80, v48
	v_mfma_f32_16x16x32_bf16 v[20:23], v[24:27], v[64:67], v[20:23]
	ds_read_b64_tr_b16 v[24:25], v135 offset:49152
	ds_read_b64_tr_b16 v[26:27], v138 offset:49152
	s_waitcnt lgkmcnt(4)
	v_mfma_f32_16x16x32_bf16 v[16:19], v[16:19], v[68:71], v[36:39]
	s_nop 2
	ds_bpermute_b32 v36, v32, v49
	ds_read_b64_tr_b16 v[34:35], v138 offset:57344
	ds_read_b64_tr_b16 v[32:33], v135 offset:57344
	s_waitcnt lgkmcnt(5)
	v_mfma_f32_16x16x32_bf16 v[16:19], v[28:31], v[64:67], v[16:19]
	ds_read_b64_tr_b16 v[28:29], v141 offset:49152
	ds_read_b64_tr_b16 v[30:31], v143 offset:49152
	s_waitcnt lgkmcnt(4)
	v_add_f32_e32 v36, v49, v36
	v_mfma_f32_16x16x32_bf16 v[24:27], v[24:27], v[68:71], v[40:43]
	v_div_scale_f32 v37, s[14:15], v36, v36, 1.0
	v_rcp_f32_e32 v38, v37
	s_waitcnt lgkmcnt(2)
	v_mfma_f32_16x16x32_bf16 v[24:27], v[32:35], v[64:67], v[24:27]
	ds_read_b64_tr_b16 v[34:35], v143 offset:57344
	ds_read_b64_tr_b16 v[32:33], v141 offset:57344
	s_add_u32 s14, s50, s62
	v_fma_f32 v39, -v37, v38, 1.0
	s_waitcnt lgkmcnt(2)
	v_mfma_f32_16x16x32_bf16 v[28:31], v[28:31], v[68:71], v[44:47]
	v_fmac_f32_e32 v38, v39, v38
	v_div_scale_f32 v39, vcc, 1.0, v36, 1.0
	v_mul_f32_e32 v40, v39, v38
	s_waitcnt lgkmcnt(0)
	v_mfma_f32_16x16x32_bf16 v[28:31], v[32:35], v[64:67], v[28:31]
	v_fma_f32 v32, -v37, v40, v39
	v_fmac_f32_e32 v40, v32, v38
	v_fma_f32 v32, -v37, v40, v39
	v_div_fmas_f32 v32, v32, v38, v40
	v_div_fixup_f32 v32, v32, v36, 1.0
	v_lshl_add_u32 v33, v125, 12, v128
	v_pk_mul_f32 v[0:1], v[0:1], v[32:33] op_sel_hi:[1,0]
	v_pk_mul_f32 v[2:3], v[2:3], v[32:33] op_sel_hi:[1,0]
	s_addc_u32 s15, s51, 0
	v_cvt_pk_bf16_f32 v0, v0, v1
	v_cvt_pk_bf16_f32 v1, v2, v3
	global_store_dwordx2 v33, v[0:1], s[14:15]
	v_pk_mul_f32 v[0:1], v[8:9], v[32:33] op_sel_hi:[1,0]
	v_pk_mul_f32 v[2:3], v[10:11], v[32:33] op_sel_hi:[1,0]
	v_cvt_pk_bf16_f32 v0, v0, v1
	v_cvt_pk_bf16_f32 v1, v2, v3
	global_store_dwordx2 v33, v[0:1], s[14:15] offset:32
	v_pk_mul_f32 v[0:1], v[4:5], v[32:33] op_sel_hi:[1,0]
	v_pk_mul_f32 v[2:3], v[6:7], v[32:33] op_sel_hi:[1,0]
	v_cvt_pk_bf16_f32 v0, v0, v1
	v_cvt_pk_bf16_f32 v1, v2, v3
	global_store_dwordx2 v33, v[0:1], s[14:15] offset:64
	v_pk_mul_f32 v[0:1], v[12:13], v[32:33] op_sel_hi:[1,0]
	v_pk_mul_f32 v[2:3], v[14:15], v[32:33] op_sel_hi:[1,0]
	v_cvt_pk_bf16_f32 v0, v0, v1
	v_cvt_pk_bf16_f32 v1, v2, v3
	global_store_dwordx2 v33, v[0:1], s[14:15] offset:96
	v_pk_mul_f32 v[0:1], v[20:21], v[32:33] op_sel_hi:[1,0]
	v_pk_mul_f32 v[2:3], v[22:23], v[32:33] op_sel_hi:[1,0]
	v_cvt_pk_bf16_f32 v0, v0, v1
	v_cvt_pk_bf16_f32 v1, v2, v3
	global_store_dwordx2 v33, v[0:1], s[14:15] offset:128
	v_pk_mul_f32 v[0:1], v[16:17], v[32:33] op_sel_hi:[1,0]
	v_pk_mul_f32 v[2:3], v[18:19], v[32:33] op_sel_hi:[1,0]
	v_cvt_pk_bf16_f32 v0, v0, v1
	v_cvt_pk_bf16_f32 v1, v2, v3
	global_store_dwordx2 v33, v[0:1], s[14:15] offset:160
	v_pk_mul_f32 v[0:1], v[24:25], v[32:33] op_sel_hi:[1,0]
	v_pk_mul_f32 v[2:3], v[26:27], v[32:33] op_sel_hi:[1,0]
	v_cvt_pk_bf16_f32 v0, v0, v1
	v_cvt_pk_bf16_f32 v1, v2, v3
	global_store_dwordx2 v33, v[0:1], s[14:15] offset:192
	v_pk_mul_f32 v[0:1], v[28:29], v[32:33] op_sel_hi:[1,0]
	v_pk_mul_f32 v[2:3], v[30:31], v[32:33] op_sel_hi:[1,0]
	v_cvt_pk_bf16_f32 v0, v0, v1
	v_cvt_pk_bf16_f32 v1, v2, v3
	s_lshl_b32 s17, s59, 7
	global_store_dwordx2 v33, v[0:1], s[14:15] offset:224
	s_add_i32 s16, s17, s89
	v_and_b32_e32 v32, 15, v126
	v_or_b32_e32 v125, s16, v32
	v_and_b32_e32 v0, -16, v126
	v_mad_u64_u32 v[8:9], s[18:19], v125, s75, v[0:1]
	v_add_u32_e32 v4, 64, v8
	v_add_u32_e32 v9, 0x80, v8
	v_add_u32_e32 v12, 0xc0, v8
	global_load_dwordx4 v[0:3], v8, s[48:49] offset:3072
	s_nop 0
	global_load_dwordx4 v[4:7], v4, s[48:49] offset:3072
	s_nop 0
	global_load_dwordx4 v[8:11], v9, s[48:49] offset:3072
	s_nop 0
	global_load_dwordx4 v[12:15], v12, s[48:49] offset:3072
	v_lshl_add_u32 v16, v125, 2, 0
	v_add_u32_e32 v16, 0x10000, v16
	ds_read_b32 v128, v16
	s_lshl_b32 s16, s59, 1
	s_or_b32 s18, s16, 1
	s_waitcnt lgkmcnt(0)
	s_waitcnt lgkmcnt(0)
	s_barrier
	s_mul_i32 s19, s18, 0x178000
	s_add_u32 s20, s0, s19
	s_addc_u32 s21, s1, 0
	v_lshl_add_u64 v[16:17], s[20:21], 0, v[104:105]
	v_add_co_u32_e32 v20, vcc, 0xbc000, v16
	s_nop 1
	v_addc_co_u32_e32 v21, vcc, 0, v17, vcc
	global_load_dwordx4 v[16:19], v[16:17], off
	s_nop 0
	global_load_dwordx4 v[20:23], v[20:21], off
	s_waitcnt vmcnt(1)
	ds_write_b128 v100, v[16:19]
	s_waitcnt vmcnt(0)
	ds_write_b128 v124, v[20:23]
	s_waitcnt lgkmcnt(0)
	s_waitcnt lgkmcnt(0)
	s_barrier
	s_and_b64 vcc, exec, s[10:11]
	s_cbranch_vccnz .LBB0_548
	s_mul_i32 s20, s59, 0x2f0000
	s_add_u32 s20, s0, s20
	s_addc_u32 s21, s1, 0
	v_lshl_add_u64 v[16:17], s[20:21], 0, v[104:105]
	s_add_u32 s20, s52, s19
	v_add_co_u32_e32 v20, vcc, 0xbc000, v16
	s_addc_u32 s21, s53, 0
	s_nop 0
	v_addc_co_u32_e32 v21, vcc, 0, v17, vcc
	v_lshl_add_u64 v[24:25], s[20:21], 0, v[104:105]
	v_add_co_u32_e32 v28, vcc, 0xbc000, v24
	global_load_dwordx4 v[16:19], v[16:17], off
	s_nop 0
	global_load_dwordx4 v[20:23], v[20:21], off
	v_addc_co_u32_e32 v29, vcc, 0, v25, vcc
	global_load_dwordx4 v[24:27], v[24:25], off
	s_nop 0
	global_load_dwordx4 v[28:31], v[28:29], off
	s_waitcnt lgkmcnt(0)
.LBB0_548:
	s_and_b64 vcc, exec, s[12:13]
	s_cbranch_vccnz .LBB0_550
	s_mul_i32 s20, s59, 0x2f0000
	s_add_u32 s20, s0, s20
	s_addc_u32 s21, s1, 0
	s_waitcnt vmcnt(3)
	v_lshl_add_u64 v[16:17], s[20:21], 0, v[104:105]
	s_add_u32 s20, s52, s19
	s_waitcnt vmcnt(2)
	v_add_co_u32_e32 v20, vcc, 0xbc000, v16
	s_addc_u32 s21, s53, 0
	s_nop 0
	v_addc_co_u32_e32 v21, vcc, 0, v17, vcc
	s_waitcnt vmcnt(1)
	v_lshl_add_u64 v[24:25], s[20:21], 0, v[104:105]
	s_waitcnt vmcnt(0)
	v_add_co_u32_e32 v28, vcc, 0xbc000, v24
	global_load_dwordx4 v[16:19], v[16:17], off
	s_nop 0
	global_load_dwordx4 v[20:23], v[20:21], off
	v_addc_co_u32_e32 v29, vcc, 0, v25, vcc
	global_load_dwordx4 v[24:27], v[24:25], off
	s_nop 0
	global_load_dwordx4 v[28:31], v[28:29], off

.LBB0_583:
	s_and_b64 vcc, exec, s[80:81]
	s_cbranch_vccz .LBB0_585
	s_waitcnt lgkmcnt(0)
.LBB0_585:
	ds_read_b64_tr_b16 v[0:1], v146 offset:49152
	ds_read_b64_tr_b16 v[2:3], v148 offset:49152
	ds_read_b64_tr_b16 v[6:7], v148 offset:57344
	ds_read_b64_tr_b16 v[4:5], v146 offset:57344
	ds_read_b64_tr_b16 v[8:9], v139 offset:49152
	ds_read_b64_tr_b16 v[10:11], v142 offset:49152
	ds_read_b64_tr_b16 v[14:15], v142 offset:57344
	ds_read_b64_tr_b16 v[12:13], v139 offset:57344
	v_lshl_add_u32 v100, v125, 12, v127
	s_waitcnt lgkmcnt(6)
	v_mfma_f32_16x16x32_bf16 v[0:3], v[0:3], v[68:71], v[60:63]
	s_mov_b64 s[10:11], 0
	s_waitcnt lgkmcnt(2)
	v_mfma_f32_16x16x32_bf16 v[8:11], v[8:11], v[68:71], v[56:59]
	v_mfma_f32_16x16x32_bf16 v[0:3], v[4:7], v[64:67], v[0:3]
	ds_read_b64_tr_b16 v[4:5], v141 offset:49152
	ds_read_b64_tr_b16 v[6:7], v145 offset:49152
	s_waitcnt lgkmcnt(2)
	v_mfma_f32_16x16x32_bf16 v[8:11], v[12:15], v[64:67], v[8:11]
	ds_read_b64_tr_b16 v[14:15], v145 offset:57344
	ds_read_b64_tr_b16 v[12:13], v141 offset:57344
	s_waitcnt vmcnt(3)
	ds_read_b64_tr_b16 v[16:17], v140 offset:49152
	ds_read_b64_tr_b16 v[18:19], v143 offset:49152
	s_waitcnt lgkmcnt(4)
	v_mfma_f32_16x16x32_bf16 v[4:7], v[4:7], v[68:71], v[52:55]
	s_waitcnt lgkmcnt(2)
	v_mfma_f32_16x16x32_bf16 v[12:15], v[12:15], v[64:67], v[4:7]
	s_nop 5
	ds_read_b64_tr_b16 v[6:7], v143 offset:57344
	ds_read_b64_tr_b16 v[4:5], v140 offset:57344
	s_waitcnt vmcnt(2)
	ds_read_b64_tr_b16 v[20:21], v147 offset:49152
	ds_read_b64_tr_b16 v[22:23], v149 offset:49152
	s_waitcnt vmcnt(1)
	ds_read_b64_tr_b16 v[26:27], v149 offset:57344
	ds_read_b64_tr_b16 v[24:25], v147 offset:57344
	s_waitcnt lgkmcnt(6)
	v_mfma_f32_16x16x32_bf16 v[16:19], v[16:19], v[68:71], v[48:51]
	s_nop 2
	v_lshlrev_b32_e32 v48, 2, v126
	s_waitcnt vmcnt(0)
	v_xor_b32_e32 v28, 64, v48
	s_waitcnt lgkmcnt(2)
	v_mfma_f32_16x16x32_bf16 v[20:23], v[20:23], v[68:71], v[32:35]
	s_nop 2
	ds_bpermute_b32 v32, v28, v150
	v_mfma_f32_16x16x32_bf16 v[16:19], v[4:7], v[64:67], v[16:19]
	ds_read_b64_tr_b16 v[4:5], v133 offset:49152
	ds_read_b64_tr_b16 v[6:7], v134 offset:49152
	ds_read_b64_tr_b16 v[30:31], v134 offset:57344
	ds_read_b64_tr_b16 v[28:29], v133 offset:57344
	s_waitcnt lgkmcnt(4)
	v_add_f32_e32 v49, v150, v32
	v_xor_b32_e32 v32, 0x80, v48
	v_mfma_f32_16x16x32_bf16 v[20:23], v[24:27], v[64:67], v[20:23]
	ds_read_b64_tr_b16 v[24:25], v135 offset:49152
	ds_read_b64_tr_b16 v[26:27], v136 offset:49152
	s_waitcnt lgkmcnt(4)
	v_mfma_f32_16x16x32_bf16 v[4:7], v[4:7], v[68:71], v[36:39]
	s_nop 2
	ds_bpermute_b32 v36, v32, v49
	ds_read_b64_tr_b16 v[34:35], v136 offset:57344
	ds_read_b64_tr_b16 v[32:33], v135 offset:57344
	s_waitcnt lgkmcnt(5)
	v_mfma_f32_16x16x32_bf16 v[28:31], v[28:31], v[64:67], v[4:7]
	s_nop 2
	ds_read_b64_tr_b16 v[4:5], v137 offset:49152
	ds_read_b64_tr_b16 v[6:7], v138 offset:49152
	s_waitcnt lgkmcnt(4)
	v_add_f32_e32 v36, v49, v36
	v_mfma_f32_16x16x32_bf16 v[24:27], v[24:27], v[68:71], v[40:43]
	v_div_scale_f32 v37, s[0:1], v36, v36, 1.0
	v_rcp_f32_e32 v38, v37
	s_waitcnt lgkmcnt(2)
	v_mfma_f32_16x16x32_bf16 v[24:27], v[32:35], v[64:67], v[24:27]
	ds_read_b64_tr_b16 v[34:35], v138 offset:57344
	ds_read_b64_tr_b16 v[32:33], v137 offset:57344
	v_fma_f32 v39, -v37, v38, 1.0
	s_waitcnt lgkmcnt(2)
	v_mfma_f32_16x16x32_bf16 v[4:7], v[4:7], v[68:71], v[44:47]
	v_fmac_f32_e32 v38, v39, v38
	v_div_scale_f32 v39, vcc, 1.0, v36, 1.0
	v_mul_f32_e32 v40, v39, v38
	s_waitcnt lgkmcnt(0)
	v_mfma_f32_16x16x32_bf16 v[32:35], v[32:35], v[64:67], v[4:7]
	s_nop 2
	v_fma_f32 v4, -v37, v40, v39
	v_fmac_f32_e32 v40, v4, v38
	v_fma_f32 v4, -v37, v40, v39
	v_div_fmas_f32 v4, v4, v38, v40
	v_div_fixup_f32 v6, v4, v36, 1.0
	v_pk_mul_f32 v[0:1], v[0:1], v[6:7] op_sel_hi:[1,0]
	v_pk_mul_f32 v[2:3], v[2:3], v[6:7] op_sel_hi:[1,0]
	v_cvt_pk_bf16_f32 v0, v0, v1
	v_cvt_pk_bf16_f32 v1, v2, v3
	global_store_dwordx2 v100, v[0:1], s[14:15]
	v_pk_mul_f32 v[0:1], v[8:9], v[6:7] op_sel_hi:[1,0]
	v_pk_mul_f32 v[2:3], v[10:11], v[6:7] op_sel_hi:[1,0]
	v_cvt_pk_bf16_f32 v0, v0, v1
	v_cvt_pk_bf16_f32 v1, v2, v3
	global_store_dwordx2 v100, v[0:1], s[14:15] offset:32
	v_pk_mul_f32 v[0:1], v[12:13], v[6:7] op_sel_hi:[1,0]
	v_pk_mul_f32 v[2:3], v[14:15], v[6:7] op_sel_hi:[1,0]
	v_cvt_pk_bf16_f32 v0, v0, v1
	v_cvt_pk_bf16_f32 v1, v2, v3
	global_store_dwordx2 v100, v[0:1], s[14:15] offset:64
	v_pk_mul_f32 v[0:1], v[16:17], v[6:7] op_sel_hi:[1,0]
	v_pk_mul_f32 v[2:3], v[18:19], v[6:7] op_sel_hi:[1,0]
	v_cvt_pk_bf16_f32 v0, v0, v1
	v_cvt_pk_bf16_f32 v1, v2, v3
	global_store_dwordx2 v100, v[0:1], s[14:15] offset:96
	v_pk_mul_f32 v[0:1], v[20:21], v[6:7] op_sel_hi:[1,0]
	v_pk_mul_f32 v[2:3], v[22:23], v[6:7] op_sel_hi:[1,0]
	v_cvt_pk_bf16_f32 v0, v0, v1
	v_cvt_pk_bf16_f32 v1, v2, v3
	global_store_dwordx2 v100, v[0:1], s[14:15] offset:128
	v_pk_mul_f32 v[0:1], v[28:29], v[6:7] op_sel_hi:[1,0]
	v_pk_mul_f32 v[2:3], v[30:31], v[6:7] op_sel_hi:[1,0]
	v_cvt_pk_bf16_f32 v0, v0, v1
	v_cvt_pk_bf16_f32 v1, v2, v3
	global_store_dwordx2 v100, v[0:1], s[14:15] offset:160
	v_pk_mul_f32 v[0:1], v[24:25], v[6:7] op_sel_hi:[1,0]
	v_pk_mul_f32 v[2:3], v[26:27], v[6:7] op_sel_hi:[1,0]
	v_cvt_pk_bf16_f32 v0, v0, v1
	v_cvt_pk_bf16_f32 v1, v2, v3
	global_store_dwordx2 v100, v[0:1], s[14:15] offset:192
	v_pk_mul_f32 v[0:1], v[32:33], v[6:7] op_sel_hi:[1,0]
	v_lshl_add_u64 v[4:5], s[14:15], 0, v[100:101]
	v_cvt_pk_bf16_f32 v0, v0, v1
	v_pk_mul_f32 v[2:3], v[34:35], v[6:7] op_sel_hi:[1,0]

.LBB0_1899:
	v_pk_add_f32 v[0:1], v[0:1], v[16:17] op_sel_hi:[1,0]
	v_pk_add_f32 v[2:3], v[2:3], v[16:17] op_sel_hi:[1,0]
	v_pk_mul_f32 v[18:19], v[0:1], s[80:81] op_sel_hi:[1,0]
	v_pk_add_f32 v[0:1], v[4:5], v[16:17] op_sel_hi:[1,0]
	v_pk_mul_f32 v[2:3], v[2:3], s[80:81] op_sel_hi:[1,0]
	v_pk_mul_f32 v[20:21], v[0:1], s[80:81] op_sel_hi:[1,0]
	v_pk_add_f32 v[0:1], v[6:7], v[16:17] op_sel_hi:[1,0]
	s_sub_i32 s10, 63, s1
	v_pk_mul_f32 v[0:1], v[0:1], s[80:81] op_sel_hi:[1,0]
	ds_write_b128 v114, v[0:3] offset:16
	v_pk_add_f32 v[0:1], v[8:9], v[16:17] op_sel_hi:[1,0]
	v_pk_add_f32 v[2:3], v[10:11], v[16:17] op_sel_hi:[1,0]
	v_pk_mul_f32 v[0:1], v[0:1], s[80:81] op_sel_hi:[1,0]
	v_pk_mul_f32 v[2:3], v[2:3], s[80:81] op_sel_hi:[1,0]
	ds_write_b128 v114, v[0:3] offset:32
	v_pk_add_f32 v[0:1], v[12:13], v[16:17] op_sel_hi:[1,0]
	v_pk_add_f32 v[2:3], v[14:15], v[16:17] op_sel_hi:[1,0]
	v_pk_mul_f32 v[0:1], v[0:1], s[80:81] op_sel_hi:[1,0]
	v_pk_mul_f32 v[2:3], v[2:3], s[80:81] op_sel_hi:[1,0]
	ds_write_b128 v114, v[18:21]
	ds_write_b128 v114, v[0:3] offset:48
	s_waitcnt lgkmcnt(0)
	s_barrier
	s_load_dwordx2 s[6:7], s[52:53], 0x108
	s_load_dwordx2 s[46:47], s[52:53], 0x138
	v_mov_b32_e32 v126, v108
	s_lshl_b32 s5, s10, 7
	s_add_i32 s0, s5, s57
	v_and_b32_e32 v32, 15, v126
	v_or_b32_e32 v125, s0, v32
	v_readlane_b32 s0, v247, 37
	s_lshl_b32 s0, s0, 1
	s_waitcnt lgkmcnt(0)
	s_add_u32 s44, s6, s0
	v_and_b32_e32 v0, -16, v126
	s_addc_u32 s45, s7, 0
	v_mad_u64_u32 v[8:9], s[6:7], v125, s59, v[0:1]
	v_add_u32_e32 v4, 64, v8
	v_add_u32_e32 v9, 0x80, v8
	v_add_u32_e32 v12, 0xc0, v8
	global_load_dwordx4 v[0:3], v8, s[44:45] offset:3072
	s_nop 0
	global_load_dwordx4 v[4:7], v4, s[44:45] offset:3072
	s_nop 0
	global_load_dwordx4 v[8:11], v9, s[44:45] offset:3072
	s_nop 0
	global_load_dwordx4 v[12:15], v12, s[44:45] offset:3072
	v_lshl_add_u32 v16, v125, 2, s79
	ds_read_b32 v127, v16
	s_lshl_b32 s4, s10, 1
	s_add_u32 s48, s44, 0x1000
	s_addc_u32 s49, s45, 0
	s_or_b32 s11, s4, 1
	s_add_u32 s68, s44, 0x1400
	s_addc_u32 s69, s45, 0
	s_waitcnt lgkmcnt(0)
	s_waitcnt lgkmcnt(0)
	s_barrier
	s_mul_i32 s12, s11, 0x178000
	s_add_u32 s6, s48, s12
	s_addc_u32 s7, s49, 0
	v_lshl_add_u64 v[20:21], s[6:7], 0, v[104:105]
	global_load_dwordx4 v[16:19], v[20:21], off
	v_add_co_u32_e32 v20, vcc, s51, v20
	v_add_u32_e32 v100, 0, v110
	s_nop 0
	v_addc_co_u32_e32 v21, vcc, 0, v21, vcc
	global_load_dwordx4 v[20:23], v[20:21], off
	v_add_u32_e32 v124, 0, v111
	s_waitcnt vmcnt(1)
	ds_write_b128 v100, v[16:19]
	s_waitcnt vmcnt(0)
	ds_write_b128 v124, v[20:23]
	s_waitcnt lgkmcnt(0)
	s_waitcnt lgkmcnt(0)
	s_barrier
	v_cndmask_b32_e64 v24, 0, 1, s[74:75]
	v_cmp_ne_u32_e64 s[6:7], 1, v24
	s_andn2_b64 vcc, exec, s[74:75]
	s_mul_i32 s10, s10, 0x2f0000
	s_cbranch_vccnz .LBB0_1901
	s_add_u32 s8, s48, s10
	s_addc_u32 s9, s49, 0
	v_lshl_add_u64 v[16:17], s[8:9], 0, v[104:105]
	s_add_u32 s8, s68, s12
	v_add_co_u32_e32 v20, vcc, 0xbc000, v16
	s_addc_u32 s9, s69, 0
	s_nop 0
	v_addc_co_u32_e32 v21, vcc, 0, v17, vcc
	v_lshl_add_u64 v[24:25], s[8:9], 0, v[104:105]
	v_add_co_u32_e32 v28, vcc, 0xbc000, v24
	global_load_dwordx4 v[16:19], v[16:17], off
	s_nop 0
	global_load_dwordx4 v[20:23], v[20:21], off
	v_addc_co_u32_e32 v29, vcc, 0, v25, vcc
	global_load_dwordx4 v[24:27], v[24:25], off
	s_nop 0
	global_load_dwordx4 v[28:31], v[28:29], off
	s_waitcnt lgkmcnt(0)
.LBB0_1901:
	v_cndmask_b32_e64 v33, 0, 1, s[72:73]
	v_cmp_ne_u32_e64 s[8:9], 1, v33
	s_andn2_b64 vcc, exec, s[72:73]
	s_cbranch_vccnz .LBB0_1903
	s_add_u32 s14, s48, s10
	s_addc_u32 s15, s49, 0
	s_waitcnt vmcnt(3)
	v_lshl_add_u64 v[16:17], s[14:15], 0, v[104:105]
	s_add_u32 s12, s68, s12
	s_waitcnt vmcnt(2)
	v_add_co_u32_e32 v20, vcc, 0xbc000, v16
	s_addc_u32 s13, s69, 0
	s_nop 0
	v_addc_co_u32_e32 v21, vcc, 0, v17, vcc
	s_waitcnt vmcnt(1)
	v_lshl_add_u64 v[24:25], s[12:13], 0, v[104:105]
	s_waitcnt vmcnt(0)
	v_add_co_u32_e32 v28, vcc, 0xbc000, v24
	global_load_dwordx4 v[16:19], v[16:17], off
	s_nop 0
	global_load_dwordx4 v[20:23], v[20:21], off
	v_addc_co_u32_e32 v29, vcc, 0, v25, vcc
	global_load_dwordx4 v[24:27], v[24:25], off
	s_nop 0
	global_load_dwordx4 v[28:31], v[28:29], off

.LBB0_1935:
	s_and_b64 vcc, exec, s[72:73]
	s_cbranch_vccz .LBB0_1937
	s_waitcnt lgkmcnt(0)
.LBB0_1937:
	ds_read_b64_tr_b16 v[0:1], v142 offset:49152
	ds_read_b64_tr_b16 v[2:3], v146 offset:49152
	ds_read_b64_tr_b16 v[6:7], v146 offset:57344
	ds_read_b64_tr_b16 v[4:5], v142 offset:57344
	ds_read_b64_tr_b16 v[8:9], v136 offset:49152
	ds_read_b64_tr_b16 v[10:11], v137 offset:49152
	ds_read_b64_tr_b16 v[14:15], v137 offset:57344
	ds_read_b64_tr_b16 v[12:13], v136 offset:57344
	s_add_u32 s10, s46, s0
	s_waitcnt lgkmcnt(6)
	v_mfma_f32_16x16x32_bf16 v[0:3], v[0:3], v[68:71], v[60:63]
	s_addc_u32 s11, s47, 0
	s_waitcnt lgkmcnt(2)
	v_mfma_f32_16x16x32_bf16 v[8:11], v[8:11], v[68:71], v[52:55]
	v_mfma_f32_16x16x32_bf16 v[0:3], v[4:7], v[64:67], v[0:3]
	ds_read_b64_tr_b16 v[4:5], v139 offset:49152
	ds_read_b64_tr_b16 v[6:7], v145 offset:49152
	s_waitcnt lgkmcnt(2)
	v_mfma_f32_16x16x32_bf16 v[8:11], v[12:15], v[64:67], v[8:11]
	ds_read_b64_tr_b16 v[14:15], v145 offset:57344
	ds_read_b64_tr_b16 v[12:13], v139 offset:57344
	s_waitcnt vmcnt(3)
	ds_read_b64_tr_b16 v[16:17], v140 offset:49152
	ds_read_b64_tr_b16 v[18:19], v147 offset:49152
	s_waitcnt lgkmcnt(4)
	v_mfma_f32_16x16x32_bf16 v[4:7], v[4:7], v[68:71], v[48:51]
	s_waitcnt lgkmcnt(2)
	v_mfma_f32_16x16x32_bf16 v[4:7], v[12:15], v[64:67], v[4:7]
	ds_read_b64_tr_b16 v[14:15], v147 offset:57344
	ds_read_b64_tr_b16 v[12:13], v140 offset:57344
	s_waitcnt vmcnt(2)
	ds_read_b64_tr_b16 v[20:21], v148 offset:49152
	ds_read_b64_tr_b16 v[22:23], v149 offset:49152
	s_waitcnt vmcnt(1)
	ds_read_b64_tr_b16 v[26:27], v149 offset:57344
	ds_read_b64_tr_b16 v[24:25], v148 offset:57344
	v_lshlrev_b32_e32 v48, 2, v126
	s_waitcnt lgkmcnt(6)
	v_mfma_f32_16x16x32_bf16 v[16:19], v[16:19], v[68:71], v[56:59]
	s_waitcnt vmcnt(0)
	v_xor_b32_e32 v28, 64, v48
	v_mov_b32_e32 v126, v108
	s_waitcnt lgkmcnt(2)
	v_mfma_f32_16x16x32_bf16 v[20:23], v[20:23], v[68:71], v[32:35]
	s_nop 2
	ds_bpermute_b32 v32, v28, v150
	v_mfma_f32_16x16x32_bf16 v[12:15], v[12:15], v[64:67], v[16:19]
	s_nop 2
	ds_read_b64_tr_b16 v[16:17], v133 offset:49152
	ds_read_b64_tr_b16 v[18:19], v134 offset:49152
	ds_read_b64_tr_b16 v[30:31], v134 offset:57344
	ds_read_b64_tr_b16 v[28:29], v133 offset:57344
	s_waitcnt lgkmcnt(4)
	v_add_f32_e32 v49, v150, v32
	v_xor_b32_e32 v32, 0x80, v48
	v_mfma_f32_16x16x32_bf16 v[20:23], v[24:27], v[64:67], v[20:23]
	ds_read_b64_tr_b16 v[24:25], v135 offset:49152
	ds_read_b64_tr_b16 v[26:27], v138 offset:49152
	s_waitcnt lgkmcnt(4)
	v_mfma_f32_16x16x32_bf16 v[16:19], v[16:19], v[68:71], v[36:39]
	s_nop 2
	ds_bpermute_b32 v36, v32, v49
	ds_read_b64_tr_b16 v[34:35], v138 offset:57344
	ds_read_b64_tr_b16 v[32:33], v135 offset:57344
	s_waitcnt lgkmcnt(5)
	v_mfma_f32_16x16x32_bf16 v[16:19], v[28:31], v[64:67], v[16:19]
	ds_read_b64_tr_b16 v[28:29], v141 offset:49152
	ds_read_b64_tr_b16 v[30:31], v143 offset:49152
	s_waitcnt lgkmcnt(4)
	v_add_f32_e32 v36, v49, v36
	v_mfma_f32_16x16x32_bf16 v[24:27], v[24:27], v[68:71], v[40:43]
	v_div_scale_f32 v37, s[4:5], v36, v36, 1.0
	v_rcp_f32_e32 v38, v37
	s_waitcnt lgkmcnt(2)
	v_mfma_f32_16x16x32_bf16 v[24:27], v[32:35], v[64:67], v[24:27]
	ds_read_b64_tr_b16 v[34:35], v143 offset:57344
	ds_read_b64_tr_b16 v[32:33], v141 offset:57344
	s_lshl_b32 s4, s1, 7
	v_fma_f32 v39, -v37, v38, 1.0
	s_waitcnt lgkmcnt(2)
	v_mfma_f32_16x16x32_bf16 v[28:31], v[28:31], v[68:71], v[44:47]
	v_fmac_f32_e32 v38, v39, v38
	v_div_scale_f32 v39, vcc, 1.0, v36, 1.0
	v_mul_f32_e32 v40, v39, v38
	s_waitcnt lgkmcnt(0)
	v_mfma_f32_16x16x32_bf16 v[28:31], v[32:35], v[64:67], v[28:31]
	v_fma_f32 v32, -v37, v40, v39
	v_fmac_f32_e32 v40, v32, v38
	v_fma_f32 v32, -v37, v40, v39
	v_div_fmas_f32 v32, v32, v38, v40
	v_div_fixup_f32 v32, v32, v36, 1.0
	v_lshl_add_u32 v33, v125, 12, v128
	v_pk_mul_f32 v[0:1], v[0:1], v[32:33] op_sel_hi:[1,0]
	v_pk_mul_f32 v[2:3], v[2:3], v[32:33] op_sel_hi:[1,0]
	v_cvt_pk_bf16_f32 v0, v0, v1
	v_cvt_pk_bf16_f32 v1, v2, v3
	global_store_dwordx2 v33, v[0:1], s[10:11]
	v_pk_mul_f32 v[0:1], v[8:9], v[32:33] op_sel_hi:[1,0]
	v_pk_mul_f32 v[2:3], v[10:11], v[32:33] op_sel_hi:[1,0]
	v_cvt_pk_bf16_f32 v0, v0, v1
	v_cvt_pk_bf16_f32 v1, v2, v3
	global_store_dwordx2 v33, v[0:1], s[10:11] offset:32
	v_pk_mul_f32 v[0:1], v[4:5], v[32:33] op_sel_hi:[1,0]
	v_pk_mul_f32 v[2:3], v[6:7], v[32:33] op_sel_hi:[1,0]
	v_cvt_pk_bf16_f32 v0, v0, v1
	v_cvt_pk_bf16_f32 v1, v2, v3
	global_store_dwordx2 v33, v[0:1], s[10:11] offset:64
	v_pk_mul_f32 v[0:1], v[12:13], v[32:33] op_sel_hi:[1,0]
	v_pk_mul_f32 v[2:3], v[14:15], v[32:33] op_sel_hi:[1,0]
	v_cvt_pk_bf16_f32 v0, v0, v1
	v_cvt_pk_bf16_f32 v1, v2, v3
	global_store_dwordx2 v33, v[0:1], s[10:11] offset:96
	v_pk_mul_f32 v[0:1], v[20:21], v[32:33] op_sel_hi:[1,0]
	v_pk_mul_f32 v[2:3], v[22:23], v[32:33] op_sel_hi:[1,0]
	v_cvt_pk_bf16_f32 v0, v0, v1
	v_cvt_pk_bf16_f32 v1, v2, v3
	global_store_dwordx2 v33, v[0:1], s[10:11] offset:128
	v_pk_mul_f32 v[0:1], v[16:17], v[32:33] op_sel_hi:[1,0]
	v_pk_mul_f32 v[2:3], v[18:19], v[32:33] op_sel_hi:[1,0]
	v_cvt_pk_bf16_f32 v0, v0, v1
	v_cvt_pk_bf16_f32 v1, v2, v3
	global_store_dwordx2 v33, v[0:1], s[10:11] offset:160
	v_pk_mul_f32 v[0:1], v[24:25], v[32:33] op_sel_hi:[1,0]
	v_pk_mul_f32 v[2:3], v[26:27], v[32:33] op_sel_hi:[1,0]
	v_cvt_pk_bf16_f32 v0, v0, v1
	v_cvt_pk_bf16_f32 v1, v2, v3
	global_store_dwordx2 v33, v[0:1], s[10:11] offset:192
	v_pk_mul_f32 v[0:1], v[28:29], v[32:33] op_sel_hi:[1,0]
	v_pk_mul_f32 v[2:3], v[30:31], v[32:33] op_sel_hi:[1,0]
	v_cvt_pk_bf16_f32 v0, v0, v1
	v_cvt_pk_bf16_f32 v1, v2, v3
	global_store_dwordx2 v33, v[0:1], s[10:11] offset:224
	s_add_i32 s0, s4, s57
	v_and_b32_e32 v32, 15, v126
	v_or_b32_e32 v125, s0, v32
	v_and_b32_e32 v0, -16, v126
	v_mad_u64_u32 v[8:9], s[12:13], v125, s59, v[0:1]
	v_add_u32_e32 v4, 64, v8
	v_add_u32_e32 v9, 0x80, v8
	v_add_u32_e32 v12, 0xc0, v8
	global_load_dwordx4 v[0:3], v8, s[44:45] offset:3072
	s_nop 0
	global_load_dwordx4 v[4:7], v4, s[44:45] offset:3072
	s_nop 0
	global_load_dwordx4 v[8:11], v9, s[44:45] offset:3072
	s_nop 0
	global_load_dwordx4 v[12:15], v12, s[44:45] offset:3072
	v_lshl_add_u32 v16, v125, 2, 0
	v_add_u32_e32 v16, 0x10000, v16
	ds_read_b32 v128, v16
	s_lshl_b32 s0, s1, 1
	s_or_b32 s5, s0, 1
	s_waitcnt lgkmcnt(0)
	s_waitcnt lgkmcnt(0)
	s_barrier
	s_mul_i32 s12, s5, 0x178000
	s_add_u32 s14, s48, s12
	s_addc_u32 s15, s49, 0
	v_lshl_add_u64 v[16:17], s[14:15], 0, v[104:105]
	v_add_co_u32_e32 v20, vcc, 0xbc000, v16
	s_nop 1
	v_addc_co_u32_e32 v21, vcc, 0, v17, vcc
	global_load_dwordx4 v[16:19], v[16:17], off
	s_nop 0
	global_load_dwordx4 v[20:23], v[20:21], off
	s_waitcnt vmcnt(1)
	ds_write_b128 v100, v[16:19]
	s_waitcnt vmcnt(0)
	ds_write_b128 v124, v[20:23]
	s_waitcnt lgkmcnt(0)
	s_waitcnt lgkmcnt(0)
	s_barrier
	s_and_b64 vcc, exec, s[6:7]
	s_cbranch_vccnz .LBB0_1939
	s_mul_i32 s13, s1, 0x2f0000
	s_add_u32 s14, s48, s13
	s_addc_u32 s15, s49, 0
	v_lshl_add_u64 v[16:17], s[14:15], 0, v[104:105]
	s_add_u32 s14, s68, s12
	v_add_co_u32_e32 v20, vcc, 0xbc000, v16
	s_addc_u32 s15, s69, 0
	s_nop 0
	v_addc_co_u32_e32 v21, vcc, 0, v17, vcc
	v_lshl_add_u64 v[24:25], s[14:15], 0, v[104:105]
	v_add_co_u32_e32 v28, vcc, 0xbc000, v24
	global_load_dwordx4 v[16:19], v[16:17], off
	s_nop 0
	global_load_dwordx4 v[20:23], v[20:21], off
	v_addc_co_u32_e32 v29, vcc, 0, v25, vcc
	global_load_dwordx4 v[24:27], v[24:25], off
	s_nop 0
	global_load_dwordx4 v[28:31], v[28:29], off
	s_waitcnt lgkmcnt(0)
.LBB0_1939:
	s_and_b64 vcc, exec, s[8:9]
	s_cbranch_vccnz .LBB0_1941
	s_mul_i32 s13, s1, 0x2f0000
	s_add_u32 s14, s48, s13
	s_addc_u32 s15, s49, 0
	s_waitcnt vmcnt(3)
	v_lshl_add_u64 v[16:17], s[14:15], 0, v[104:105]
	s_add_u32 s12, s68, s12
	s_waitcnt vmcnt(2)
	v_add_co_u32_e32 v20, vcc, 0xbc000, v16
	s_addc_u32 s13, s69, 0
	s_nop 0
	v_addc_co_u32_e32 v21, vcc, 0, v17, vcc
	s_waitcnt vmcnt(1)
	v_lshl_add_u64 v[24:25], s[12:13], 0, v[104:105]
	s_waitcnt vmcnt(0)
	v_add_co_u32_e32 v28, vcc, 0xbc000, v24
	global_load_dwordx4 v[16:19], v[16:17], off
	s_nop 0
	global_load_dwordx4 v[20:23], v[20:21], off
	v_addc_co_u32_e32 v29, vcc, 0, v25, vcc
	global_load_dwordx4 v[24:27], v[24:25], off
	s_nop 0
	global_load_dwordx4 v[28:31], v[28:29], off

.LBB0_1974:
	s_and_b64 vcc, exec, s[72:73]
	s_cbranch_vccz .LBB0_1976
	s_waitcnt lgkmcnt(0)
.LBB0_1976:
	ds_read_b64_tr_b16 v[0:1], v146 offset:49152
	ds_read_b64_tr_b16 v[2:3], v148 offset:49152
	ds_read_b64_tr_b16 v[6:7], v148 offset:57344
	ds_read_b64_tr_b16 v[4:5], v146 offset:57344
	ds_read_b64_tr_b16 v[8:9], v139 offset:49152
	ds_read_b64_tr_b16 v[10:11], v142 offset:49152
	ds_read_b64_tr_b16 v[14:15], v142 offset:57344
	ds_read_b64_tr_b16 v[12:13], v139 offset:57344
	v_lshl_add_u32 v100, v125, 12, v127
	s_waitcnt lgkmcnt(6)
	v_mfma_f32_16x16x32_bf16 v[0:3], v[0:3], v[68:71], v[60:63]
	s_mov_b64 s[6:7], 0
	s_waitcnt lgkmcnt(2)
	v_mfma_f32_16x16x32_bf16 v[8:11], v[8:11], v[68:71], v[56:59]
	v_mfma_f32_16x16x32_bf16 v[0:3], v[4:7], v[64:67], v[0:3]
	ds_read_b64_tr_b16 v[4:5], v141 offset:49152
	ds_read_b64_tr_b16 v[6:7], v145 offset:49152
	s_waitcnt lgkmcnt(2)
	v_mfma_f32_16x16x32_bf16 v[8:11], v[12:15], v[64:67], v[8:11]
	ds_read_b64_tr_b16 v[14:15], v145 offset:57344
	ds_read_b64_tr_b16 v[12:13], v141 offset:57344
	s_waitcnt vmcnt(3)
	ds_read_b64_tr_b16 v[16:17], v140 offset:49152
	ds_read_b64_tr_b16 v[18:19], v143 offset:49152
	s_waitcnt lgkmcnt(4)
	v_mfma_f32_16x16x32_bf16 v[4:7], v[4:7], v[68:71], v[52:55]
	s_waitcnt lgkmcnt(2)
	v_mfma_f32_16x16x32_bf16 v[12:15], v[12:15], v[64:67], v[4:7]
	s_nop 5
	ds_read_b64_tr_b16 v[6:7], v143 offset:57344
	ds_read_b64_tr_b16 v[4:5], v140 offset:57344
	s_waitcnt vmcnt(2)
	ds_read_b64_tr_b16 v[20:21], v147 offset:49152
	ds_read_b64_tr_b16 v[22:23], v149 offset:49152
	s_waitcnt vmcnt(1)
	ds_read_b64_tr_b16 v[26:27], v149 offset:57344
	ds_read_b64_tr_b16 v[24:25], v147 offset:57344
	s_waitcnt lgkmcnt(6)
	v_mfma_f32_16x16x32_bf16 v[16:19], v[16:19], v[68:71], v[48:51]
	s_nop 2
	v_lshlrev_b32_e32 v48, 2, v126
	s_waitcnt vmcnt(0)
	v_xor_b32_e32 v28, 64, v48
	s_waitcnt lgkmcnt(2)
	v_mfma_f32_16x16x32_bf16 v[20:23], v[20:23], v[68:71], v[32:35]
	s_nop 2
	ds_bpermute_b32 v32, v28, v150
	v_mfma_f32_16x16x32_bf16 v[16:19], v[4:7], v[64:67], v[16:19]
	ds_read_b64_tr_b16 v[4:5], v133 offset:49152
	ds_read_b64_tr_b16 v[6:7], v134 offset:49152
	ds_read_b64_tr_b16 v[30:31], v134 offset:57344
	ds_read_b64_tr_b16 v[28:29], v133 offset:57344
	s_waitcnt lgkmcnt(4)
	v_add_f32_e32 v49, v150, v32
	v_xor_b32_e32 v32, 0x80, v48
	v_mfma_f32_16x16x32_bf16 v[20:23], v[24:27], v[64:67], v[20:23]
	ds_read_b64_tr_b16 v[24:25], v135 offset:49152
	ds_read_b64_tr_b16 v[26:27], v136 offset:49152
	s_waitcnt lgkmcnt(4)
	v_mfma_f32_16x16x32_bf16 v[4:7], v[4:7], v[68:71], v[36:39]
	s_nop 2
	ds_bpermute_b32 v36, v32, v49
	ds_read_b64_tr_b16 v[34:35], v136 offset:57344
	ds_read_b64_tr_b16 v[32:33], v135 offset:57344
	s_waitcnt lgkmcnt(5)
	v_mfma_f32_16x16x32_bf16 v[28:31], v[28:31], v[64:67], v[4:7]
	s_nop 2
	ds_read_b64_tr_b16 v[4:5], v137 offset:49152
	ds_read_b64_tr_b16 v[6:7], v138 offset:49152
	s_waitcnt lgkmcnt(4)
	v_add_f32_e32 v36, v49, v36
	v_mfma_f32_16x16x32_bf16 v[24:27], v[24:27], v[68:71], v[40:43]
	v_div_scale_f32 v37, s[4:5], v36, v36, 1.0
	v_rcp_f32_e32 v38, v37
	s_waitcnt lgkmcnt(2)
	v_mfma_f32_16x16x32_bf16 v[24:27], v[32:35], v[64:67], v[24:27]
	ds_read_b64_tr_b16 v[34:35], v138 offset:57344
	ds_read_b64_tr_b16 v[32:33], v137 offset:57344
	v_fma_f32 v39, -v37, v38, 1.0
	s_waitcnt lgkmcnt(2)
	v_mfma_f32_16x16x32_bf16 v[4:7], v[4:7], v[68:71], v[44:47]
	v_fmac_f32_e32 v38, v39, v38
	v_div_scale_f32 v39, vcc, 1.0, v36, 1.0
	v_mul_f32_e32 v40, v39, v38
	s_waitcnt lgkmcnt(0)
	v_mfma_f32_16x16x32_bf16 v[32:35], v[32:35], v[64:67], v[4:7]
	s_nop 2
	v_fma_f32 v4, -v37, v40, v39
	v_fmac_f32_e32 v40, v4, v38
	v_fma_f32 v4, -v37, v40, v39
	v_div_fmas_f32 v4, v4, v38, v40
	v_div_fixup_f32 v6, v4, v36, 1.0
	v_pk_mul_f32 v[0:1], v[0:1], v[6:7] op_sel_hi:[1,0]
	v_pk_mul_f32 v[2:3], v[2:3], v[6:7] op_sel_hi:[1,0]
	v_cvt_pk_bf16_f32 v0, v0, v1
	v_cvt_pk_bf16_f32 v1, v2, v3
	global_store_dwordx2 v100, v[0:1], s[10:11]
	v_pk_mul_f32 v[0:1], v[8:9], v[6:7] op_sel_hi:[1,0]
	v_pk_mul_f32 v[2:3], v[10:11], v[6:7] op_sel_hi:[1,0]
	v_cvt_pk_bf16_f32 v0, v0, v1
	v_cvt_pk_bf16_f32 v1, v2, v3
	global_store_dwordx2 v100, v[0:1], s[10:11] offset:32
	v_pk_mul_f32 v[0:1], v[12:13], v[6:7] op_sel_hi:[1,0]
	v_pk_mul_f32 v[2:3], v[14:15], v[6:7] op_sel_hi:[1,0]
	v_cvt_pk_bf16_f32 v0, v0, v1
	v_cvt_pk_bf16_f32 v1, v2, v3
	global_store_dwordx2 v100, v[0:1], s[10:11] offset:64
	v_pk_mul_f32 v[0:1], v[16:17], v[6:7] op_sel_hi:[1,0]
	v_pk_mul_f32 v[2:3], v[18:19], v[6:7] op_sel_hi:[1,0]
	v_cvt_pk_bf16_f32 v0, v0, v1
	v_cvt_pk_bf16_f32 v1, v2, v3
	global_store_dwordx2 v100, v[0:1], s[10:11] offset:96
	v_pk_mul_f32 v[0:1], v[20:21], v[6:7] op_sel_hi:[1,0]
	v_pk_mul_f32 v[2:3], v[22:23], v[6:7] op_sel_hi:[1,0]
	v_cvt_pk_bf16_f32 v0, v0, v1
	v_cvt_pk_bf16_f32 v1, v2, v3
	global_store_dwordx2 v100, v[0:1], s[10:11] offset:128
	v_pk_mul_f32 v[0:1], v[28:29], v[6:7] op_sel_hi:[1,0]
	v_pk_mul_f32 v[2:3], v[30:31], v[6:7] op_sel_hi:[1,0]
	v_cvt_pk_bf16_f32 v0, v0, v1
	v_cvt_pk_bf16_f32 v1, v2, v3
	global_store_dwordx2 v100, v[0:1], s[10:11] offset:160
	v_pk_mul_f32 v[0:1], v[24:25], v[6:7] op_sel_hi:[1,0]
	v_pk_mul_f32 v[2:3], v[26:27], v[6:7] op_sel_hi:[1,0]
	v_cvt_pk_bf16_f32 v0, v0, v1
	v_cvt_pk_bf16_f32 v1, v2, v3
	global_store_dwordx2 v100, v[0:1], s[10:11] offset:192
	v_pk_mul_f32 v[0:1], v[32:33], v[6:7] op_sel_hi:[1,0]
	v_lshl_add_u64 v[4:5], s[10:11], 0, v[100:101]
	v_cvt_pk_bf16_f32 v0, v0, v1
	v_pk_mul_f32 v[2:3], v[34:35], v[6:7] op_sel_hi:[1,0]
